# grid barriers: flat release - all workgroups wait on the top counter directly instead of top-generation word relayed through per-XCD generation words
# speedup vs baseline: 1.0110x; 1.0110x over previous
; __device__ __forceinline__ unsigned xb_ld(unsigned* p)              { return __hip_atomic_load(p, __ATOMIC_RELAXED, __HIP_MEMORY_SCOPE_AGENT); }
; __device__ __forceinline__ unsigned xb_add(unsigned* p, unsigned v) { return __hip_atomic_fetch_add(p, v, __ATOMIC_RELAXED, __HIP_MEMORY_SCOPE_AGENT); }
; #define XB_SPIN(cond, bar) do { unsigned _sp = 0; while (cond) { __builtin_amdgcn_s_sleep(1); \
;     if ((++_sp & 255u) == 0u) { if (xb_ld(&(bar)[XB_TMO])) break; if (_sp > XB_SPIN_CAP) { atomicAdd(&(bar)[XB_TMO], 1u); break; } } } } while (0)
; __device__ __forceinline__ void xcd_barrier(const XcdBarrier& b, const int tid) {
;     ...
;         const unsigned old = xb_add(&bar[XB_XSUB(b.x)], 1u);
;         const unsigned gen = old / nloc;
;         if (old + 1u == (gen + 1u) * nloc) {
;             __builtin_amdgcn_fence(__ATOMIC_RELEASE, "agent");
;             asm volatile("s_waitcnt vmcnt(0)" ::: "memory");
;             const unsigned og = xb_add(&bar[XB_TOP], 1u);
;             const unsigned tg = og / nx;
;             if (og + 1u == (tg + 1u) * nx) xb_add(&bar[XB_TOPGEN], 1u);
;             else XB_SPIN(xb_ld(&bar[XB_TOPGEN]) == tg, bar);
;             __builtin_amdgcn_fence(__ATOMIC_ACQUIRE, "agent");
;             xb_add(&bar[XB_XGEN(b.x)], 1u);
;             asm volatile("s_waitcnt vmcnt(0)" ::: "memory");
;         } else {
;             XB_SPIN(xb_ld(&bar[XB_XGEN(b.x)]) == gen, bar);
;             __builtin_amdgcn_fence(__ATOMIC_ACQUIRE, "agent");
;             asm volatile("s_waitcnt vmcnt(0)" ::: "memory");
;         }
;     }
;     __syncthreads();
.LBB0_79:
	s_or_b64 exec, exec, s[16:17]
	v_cvt_f32_u32_e32 v4, v2
	s_waitcnt vmcnt(0)
	v_readfirstlane_b32 s12, v3
	v_sub_u32_e32 v3, 0, v2
	v_rcp_iflag_f32_e32 v4, v4
	v_add_u32_e32 v5, s12, v1
	v_mul_f32_e32 v4, 0x4f7ffffe, v4
	v_cvt_u32_f32_e32 v4, v4
	v_mul_lo_u32 v1, v3, v4
	v_mul_hi_u32 v1, v4, v1
	v_add_u32_e32 v1, v4, v1
	v_mul_hi_u32 v1, v5, v1
	v_mul_lo_u32 v3, v1, v2
	v_sub_u32_e32 v3, v5, v3
	v_add_u32_e32 v4, 1, v1
	v_cmp_ge_u32_e32 vcc, v3, v2
	s_nop 1
	v_cndmask_b32_e32 v1, v1, v4, vcc
	v_sub_u32_e32 v4, v3, v2
	v_cndmask_b32_e32 v3, v3, v4, vcc
	v_add_u32_e32 v4, 1, v1
	v_cmp_ge_u32_e32 vcc, v3, v2
	v_add_u32_e32 v3, 1, v5
	s_nop 0
	v_cndmask_b32_e32 v1, v1, v4, vcc
	v_mul_lo_u32 v4, v2, v1
	v_add_u32_e32 v2, v4, v2
	s_waitcnt lgkmcnt(0)
	v_add_u32_e32 v4, 1, v1
	v_mul_lo_u32 v4, v4, v0
	v_mov_b32_e32 v5, 0x3000
	v_cmp_ne_u32_e32 vcc, v3, v2
	s_cbranch_vccnz .Lgb0_wait
	buffer_wbl2 sc1
	s_waitcnt vmcnt(0) lgkmcnt(0)
	v_mov_b32_e32 v2, 1
	global_atomic_add v5, v2, s[26:27] offset:1024
.Lgb0_wait:
	s_cmpk_lg_i32 s3, 0x100
	s_cbranch_scc1 .Lgb0_spin0
	s_cmpk_ge_i32 s2, 0xa0
	s_cbranch_scc1 .Lgb0_out
.Lgb0_spin0:
	s_mov_b32 s33, 0
.Lgb0_spin:
	global_load_dword v3, v5, s[26:27] offset:1024 sc1
	s_waitcnt vmcnt(0)
	v_cmp_ge_u32_e32 vcc, v3, v4
	s_cbranch_vccnz .Lgb0_done
	s_sleep 1
	s_add_i32 s33, s33, 1
	s_cmp_lt_u32 s33, 0x8000
	s_cbranch_scc1 .Lgb0_spin
.Lgb0_done:
	buffer_inv sc1
.Lgb0_out:
	s_waitcnt vmcnt(0)
.LBB0_113:
	s_or_b64 exec, exec, s[0:1]
	s_waitcnt lgkmcnt(0)
	s_barrier

; __device__ __forceinline__ unsigned xb_ld(unsigned* p)              { return __hip_atomic_load(p, __ATOMIC_RELAXED, __HIP_MEMORY_SCOPE_AGENT); }
; __device__ __forceinline__ unsigned xb_add(unsigned* p, unsigned v) { return __hip_atomic_fetch_add(p, v, __ATOMIC_RELAXED, __HIP_MEMORY_SCOPE_AGENT); }
; #define XB_SPIN(cond, bar) do { unsigned _sp = 0; while (cond) { __builtin_amdgcn_s_sleep(1); \
;     if ((++_sp & 255u) == 0u) { if (xb_ld(&(bar)[XB_TMO])) break; if (_sp > XB_SPIN_CAP) { atomicAdd(&(bar)[XB_TMO], 1u); break; } } } } while (0)
; __device__ __forceinline__ void xcd_barrier(const XcdBarrier& b, const int tid) {
;     ...
;         const unsigned old = xb_add(&bar[XB_XSUB(b.x)], 1u);
;         const unsigned gen = old / nloc;
;         if (old + 1u == (gen + 1u) * nloc) {
;             __builtin_amdgcn_fence(__ATOMIC_RELEASE, "agent");
;             asm volatile("s_waitcnt vmcnt(0)" ::: "memory");
;             const unsigned og = xb_add(&bar[XB_TOP], 1u);
;             const unsigned tg = og / nx;
;             if (og + 1u == (tg + 1u) * nx) xb_add(&bar[XB_TOPGEN], 1u);
;             else XB_SPIN(xb_ld(&bar[XB_TOPGEN]) == tg, bar);
.LBB0_169:
	s_or_b64 exec, exec, s[22:23]
	v_cvt_f32_u32_e32 v4, v2
	s_waitcnt vmcnt(0)
	v_readfirstlane_b32 s20, v3
	v_sub_u32_e32 v3, 0, v2
	v_rcp_iflag_f32_e32 v4, v4
	v_add_u32_e32 v5, s20, v1
	v_mul_f32_e32 v4, 0x4f7ffffe, v4
	v_cvt_u32_f32_e32 v4, v4
	v_mul_lo_u32 v1, v3, v4
	v_mul_hi_u32 v1, v4, v1
	v_add_u32_e32 v1, v4, v1
	v_mul_hi_u32 v1, v5, v1
	v_mul_lo_u32 v3, v1, v2
	v_sub_u32_e32 v3, v5, v3
	v_add_u32_e32 v4, 1, v1
	v_cmp_ge_u32_e32 vcc, v3, v2
	s_nop 1
	v_cndmask_b32_e32 v1, v1, v4, vcc
	v_sub_u32_e32 v4, v3, v2
	v_cndmask_b32_e32 v3, v3, v4, vcc
	v_add_u32_e32 v4, 1, v1
	v_cmp_ge_u32_e32 vcc, v3, v2
	v_add_u32_e32 v3, 1, v5
	s_nop 0
	v_cndmask_b32_e32 v1, v1, v4, vcc
	v_mul_lo_u32 v4, v2, v1
	v_add_u32_e32 v2, v4, v2
	s_waitcnt lgkmcnt(0)
	v_add_u32_e32 v4, 1, v1
	v_mul_lo_u32 v4, v4, v0
	v_mov_b32_e32 v5, 0x3000
	v_cmp_ne_u32_e32 vcc, v3, v2
	s_cbranch_vccnz .Lgb1_wait
	buffer_wbl2 sc1
	s_waitcnt vmcnt(0) lgkmcnt(0)
	v_mov_b32_e32 v2, 1
	global_atomic_add v5, v2, s[26:27] offset:1024

; __device__ __forceinline__ unsigned xb_ld(unsigned* p)              { return __hip_atomic_load(p, __ATOMIC_RELAXED, __HIP_MEMORY_SCOPE_AGENT); }
; __device__ __forceinline__ unsigned xb_add(unsigned* p, unsigned v) { return __hip_atomic_fetch_add(p, v, __ATOMIC_RELAXED, __HIP_MEMORY_SCOPE_AGENT); }
; #define XB_SPIN(cond, bar) do { unsigned _sp = 0; while (cond) { __builtin_amdgcn_s_sleep(1); \
;     if ((++_sp & 255u) == 0u) { if (xb_ld(&(bar)[XB_TMO])) break; if (_sp > XB_SPIN_CAP) { atomicAdd(&(bar)[XB_TMO], 1u); break; } } } } while (0)
; __device__ __forceinline__ void xcd_barrier(const XcdBarrier& b, const int tid) {
;     ...
;             else XB_SPIN(xb_ld(&bar[XB_TOPGEN]) == tg, bar);
;             __builtin_amdgcn_fence(__ATOMIC_ACQUIRE, "agent");
;             xb_add(&bar[XB_XGEN(b.x)], 1u);
;             asm volatile("s_waitcnt vmcnt(0)" ::: "memory");
;         } else {
;             XB_SPIN(xb_ld(&bar[XB_XGEN(b.x)]) == gen, bar);
;             __builtin_amdgcn_fence(__ATOMIC_ACQUIRE, "agent");
;             asm volatile("s_waitcnt vmcnt(0)" ::: "memory");
;         }
;     }
;     __syncthreads();
.Lgb1_out:
	s_waitcnt vmcnt(0)
.LBB0_203:
	s_or_b64 exec, exec, s[0:1]
	s_waitcnt lgkmcnt(0)
	s_barrier

; __device__ __forceinline__ unsigned xb_ld(unsigned* p)              { return __hip_atomic_load(p, __ATOMIC_RELAXED, __HIP_MEMORY_SCOPE_AGENT); }
; __device__ __forceinline__ unsigned xb_add(unsigned* p, unsigned v) { return __hip_atomic_fetch_add(p, v, __ATOMIC_RELAXED, __HIP_MEMORY_SCOPE_AGENT); }
; #define XB_SPIN(cond, bar) do { unsigned _sp = 0; while (cond) { __builtin_amdgcn_s_sleep(1); \
;     if ((++_sp & 255u) == 0u) { if (xb_ld(&(bar)[XB_TMO])) break; if (_sp > XB_SPIN_CAP) { atomicAdd(&(bar)[XB_TMO], 1u); break; } } } } while (0)
; __device__ __forceinline__ void xcd_barrier(const XcdBarrier& b, const int tid) {
;     ...
;         const unsigned old = xb_add(&bar[XB_XSUB(b.x)], 1u);
;         const unsigned gen = old / nloc;
;         if (old + 1u == (gen + 1u) * nloc) {
;             __builtin_amdgcn_fence(__ATOMIC_RELEASE, "agent");
;             asm volatile("s_waitcnt vmcnt(0)" ::: "memory");
;             const unsigned og = xb_add(&bar[XB_TOP], 1u);
;             const unsigned tg = og / nx;
;             if (og + 1u == (tg + 1u) * nx) xb_add(&bar[XB_TOPGEN], 1u);
;             else XB_SPIN(xb_ld(&bar[XB_TOPGEN]) == tg, bar);
.LBB0_433:
	s_or_b64 exec, exec, s[12:13]
	v_cvt_f32_u32_e32 v4, v2
	s_waitcnt vmcnt(0)
	v_readfirstlane_b32 s6, v3
	v_sub_u32_e32 v3, 0, v2
	v_rcp_iflag_f32_e32 v4, v4
	v_add_u32_e32 v5, s6, v1
	v_mul_f32_e32 v4, 0x4f7ffffe, v4
	v_cvt_u32_f32_e32 v4, v4
	v_mul_lo_u32 v1, v3, v4
	v_mul_hi_u32 v1, v4, v1
	v_add_u32_e32 v1, v4, v1
	v_mul_hi_u32 v1, v5, v1
	v_mul_lo_u32 v3, v1, v2
	v_sub_u32_e32 v3, v5, v3
	v_add_u32_e32 v4, 1, v1
	v_cmp_ge_u32_e32 vcc, v3, v2
	s_nop 1
	v_cndmask_b32_e32 v1, v1, v4, vcc
	v_sub_u32_e32 v4, v3, v2
	v_cndmask_b32_e32 v3, v3, v4, vcc
	v_add_u32_e32 v4, 1, v1
	v_cmp_ge_u32_e32 vcc, v3, v2
	v_add_u32_e32 v3, 1, v5
	s_nop 0
	v_cndmask_b32_e32 v1, v1, v4, vcc
	v_mul_lo_u32 v4, v2, v1
	v_add_u32_e32 v2, v4, v2
	s_waitcnt lgkmcnt(0)
	v_add_u32_e32 v4, 1, v1
	v_mul_lo_u32 v4, v4, v0
	v_mov_b32_e32 v5, 0x3000
	v_cmp_ne_u32_e32 vcc, v3, v2
	s_cbranch_vccnz .Lgb2_wait
	buffer_wbl2 sc1
	s_waitcnt vmcnt(0) lgkmcnt(0)
	v_mov_b32_e32 v2, 1
	global_atomic_add v5, v2, s[26:27] offset:1024

; __device__ __forceinline__ unsigned xb_ld(unsigned* p)              { return __hip_atomic_load(p, __ATOMIC_RELAXED, __HIP_MEMORY_SCOPE_AGENT); }
; __device__ __forceinline__ unsigned xb_add(unsigned* p, unsigned v) { return __hip_atomic_fetch_add(p, v, __ATOMIC_RELAXED, __HIP_MEMORY_SCOPE_AGENT); }
; #define XB_SPIN(cond, bar) do { unsigned _sp = 0; while (cond) { __builtin_amdgcn_s_sleep(1); \
;     if ((++_sp & 255u) == 0u) { if (xb_ld(&(bar)[XB_TMO])) break; if (_sp > XB_SPIN_CAP) { atomicAdd(&(bar)[XB_TMO], 1u); break; } } } } while (0)
; __device__ __forceinline__ void xcd_barrier(const XcdBarrier& b, const int tid) {
;     ...
;             else XB_SPIN(xb_ld(&bar[XB_TOPGEN]) == tg, bar);
;             __builtin_amdgcn_fence(__ATOMIC_ACQUIRE, "agent");
;             xb_add(&bar[XB_XGEN(b.x)], 1u);
;             asm volatile("s_waitcnt vmcnt(0)" ::: "memory");
;         } else {
;             XB_SPIN(xb_ld(&bar[XB_XGEN(b.x)]) == gen, bar);
;             __builtin_amdgcn_fence(__ATOMIC_ACQUIRE, "agent");
;             asm volatile("s_waitcnt vmcnt(0)" ::: "memory");
;         }
;     }
;     __syncthreads();
.Lgb2_out:
	s_waitcnt vmcnt(0)
.LBB0_467:
	s_or_b64 exec, exec, s[0:1]
	s_waitcnt lgkmcnt(0)
	s_barrier

; __device__ __forceinline__ unsigned xb_ld(unsigned* p)              { return __hip_atomic_load(p, __ATOMIC_RELAXED, __HIP_MEMORY_SCOPE_AGENT); }
; __device__ __forceinline__ unsigned xb_add(unsigned* p, unsigned v) { return __hip_atomic_fetch_add(p, v, __ATOMIC_RELAXED, __HIP_MEMORY_SCOPE_AGENT); }
; #define XB_SPIN(cond, bar) do { unsigned _sp = 0; while (cond) { __builtin_amdgcn_s_sleep(1); \
;     if ((++_sp & 255u) == 0u) { if (xb_ld(&(bar)[XB_TMO])) break; if (_sp > XB_SPIN_CAP) { atomicAdd(&(bar)[XB_TMO], 1u); break; } } } } while (0)
; __device__ __forceinline__ void xcd_barrier(const XcdBarrier& b, const int tid) {
;     ...
;         const unsigned old = xb_add(&bar[XB_XSUB(b.x)], 1u);
;         const unsigned gen = old / nloc;
;         if (old + 1u == (gen + 1u) * nloc) {
;             __builtin_amdgcn_fence(__ATOMIC_RELEASE, "agent");
;             asm volatile("s_waitcnt vmcnt(0)" ::: "memory");
;             const unsigned og = xb_add(&bar[XB_TOP], 1u);
;             const unsigned tg = og / nx;
;             if (og + 1u == (tg + 1u) * nx) xb_add(&bar[XB_TOPGEN], 1u);
;             else XB_SPIN(xb_ld(&bar[XB_TOPGEN]) == tg, bar);
.LBB0_512:
	s_or_b64 exec, exec, s[8:9]
	v_cvt_f32_u32_e32 v4, v2
	s_waitcnt vmcnt(0)
	v_readfirstlane_b32 s6, v3
	v_sub_u32_e32 v3, 0, v2
	v_rcp_iflag_f32_e32 v4, v4
	v_add_u32_e32 v5, s6, v1
	v_mul_f32_e32 v4, 0x4f7ffffe, v4
	v_cvt_u32_f32_e32 v4, v4
	v_mul_lo_u32 v1, v3, v4
	v_mul_hi_u32 v1, v4, v1
	v_add_u32_e32 v1, v4, v1
	v_mul_hi_u32 v1, v5, v1
	v_mul_lo_u32 v3, v1, v2
	v_sub_u32_e32 v3, v5, v3
	v_add_u32_e32 v4, 1, v1
	v_cmp_ge_u32_e32 vcc, v3, v2
	s_nop 1
	v_cndmask_b32_e32 v1, v1, v4, vcc
	v_sub_u32_e32 v4, v3, v2
	v_cndmask_b32_e32 v3, v3, v4, vcc
	v_add_u32_e32 v4, 1, v1
	v_cmp_ge_u32_e32 vcc, v3, v2
	v_add_u32_e32 v3, 1, v5
	s_nop 0
	v_cndmask_b32_e32 v1, v1, v4, vcc
	v_mul_lo_u32 v4, v2, v1
	v_add_u32_e32 v2, v4, v2
	s_waitcnt lgkmcnt(0)
	v_add_u32_e32 v4, 1, v1
	v_mul_lo_u32 v4, v4, v0
	v_mov_b32_e32 v5, 0x3000
	v_cmp_ne_u32_e32 vcc, v3, v2
	s_cbranch_vccnz .Lgb3_wait
	buffer_wbl2 sc1
	s_waitcnt vmcnt(0) lgkmcnt(0)
	v_mov_b32_e32 v2, 1
	global_atomic_add v5, v2, s[26:27] offset:1024

; __device__ __forceinline__ unsigned xb_ld(unsigned* p)              { return __hip_atomic_load(p, __ATOMIC_RELAXED, __HIP_MEMORY_SCOPE_AGENT); }
; __device__ __forceinline__ unsigned xb_add(unsigned* p, unsigned v) { return __hip_atomic_fetch_add(p, v, __ATOMIC_RELAXED, __HIP_MEMORY_SCOPE_AGENT); }
; #define XB_SPIN(cond, bar) do { unsigned _sp = 0; while (cond) { __builtin_amdgcn_s_sleep(1); \
;     if ((++_sp & 255u) == 0u) { if (xb_ld(&(bar)[XB_TMO])) break; if (_sp > XB_SPIN_CAP) { atomicAdd(&(bar)[XB_TMO], 1u); break; } } } } while (0)
; __device__ __forceinline__ void xcd_barrier(const XcdBarrier& b, const int tid) {
;     ...
;             else XB_SPIN(xb_ld(&bar[XB_TOPGEN]) == tg, bar);
;             __builtin_amdgcn_fence(__ATOMIC_ACQUIRE, "agent");
;             xb_add(&bar[XB_XGEN(b.x)], 1u);
;             asm volatile("s_waitcnt vmcnt(0)" ::: "memory");
;         } else {
;             XB_SPIN(xb_ld(&bar[XB_XGEN(b.x)]) == gen, bar);
;             __builtin_amdgcn_fence(__ATOMIC_ACQUIRE, "agent");
;             asm volatile("s_waitcnt vmcnt(0)" ::: "memory");
;         }
;     }
;     __syncthreads();
.Lgb3_out:
	s_waitcnt vmcnt(0)
.LBB0_546:
	s_or_b64 exec, exec, s[0:1]
	s_waitcnt lgkmcnt(0)
	s_barrier

; __device__ __forceinline__ unsigned xb_ld(unsigned* p)              { return __hip_atomic_load(p, __ATOMIC_RELAXED, __HIP_MEMORY_SCOPE_AGENT); }
; __device__ __forceinline__ unsigned xb_add(unsigned* p, unsigned v) { return __hip_atomic_fetch_add(p, v, __ATOMIC_RELAXED, __HIP_MEMORY_SCOPE_AGENT); }
; #define XB_SPIN(cond, bar) do { unsigned _sp = 0; while (cond) { __builtin_amdgcn_s_sleep(1); \
;     if ((++_sp & 255u) == 0u) { if (xb_ld(&(bar)[XB_TMO])) break; if (_sp > XB_SPIN_CAP) { atomicAdd(&(bar)[XB_TMO], 1u); break; } } } } while (0)
; __device__ __forceinline__ void xcd_barrier(const XcdBarrier& b, const int tid) {
;     ...
;             else XB_SPIN(xb_ld(&bar[XB_TOPGEN]) == tg, bar);
;             __builtin_amdgcn_fence(__ATOMIC_ACQUIRE, "agent");
;             xb_add(&bar[XB_XGEN(b.x)], 1u);
;             asm volatile("s_waitcnt vmcnt(0)" ::: "memory");
;         } else {
;             XB_SPIN(xb_ld(&bar[XB_XGEN(b.x)]) == gen, bar);
;             __builtin_amdgcn_fence(__ATOMIC_ACQUIRE, "agent");
;             asm volatile("s_waitcnt vmcnt(0)" ::: "memory");
;         }
;     }
;     __syncthreads();
.Lgb4_out:
	s_waitcnt vmcnt(0)
.LBB0_670:
	s_or_b64 exec, exec, s[0:1]
	s_waitcnt lgkmcnt(0)
	s_barrier

; __device__ __forceinline__ unsigned xb_ld(unsigned* p)              { return __hip_atomic_load(p, __ATOMIC_RELAXED, __HIP_MEMORY_SCOPE_AGENT); }
; __device__ __forceinline__ unsigned xb_add(unsigned* p, unsigned v) { return __hip_atomic_fetch_add(p, v, __ATOMIC_RELAXED, __HIP_MEMORY_SCOPE_AGENT); }
; #define XB_SPIN(cond, bar) do { unsigned _sp = 0; while (cond) { __builtin_amdgcn_s_sleep(1); \
;     if ((++_sp & 255u) == 0u) { if (xb_ld(&(bar)[XB_TMO])) break; if (_sp > XB_SPIN_CAP) { atomicAdd(&(bar)[XB_TMO], 1u); break; } } } } while (0)
; __device__ __forceinline__ void xcd_barrier(const XcdBarrier& b, const int tid) {
;     ...
;         const unsigned old = xb_add(&bar[XB_XSUB(b.x)], 1u);
;         const unsigned gen = old / nloc;
;         if (old + 1u == (gen + 1u) * nloc) {
;             __builtin_amdgcn_fence(__ATOMIC_RELEASE, "agent");
;             asm volatile("s_waitcnt vmcnt(0)" ::: "memory");
;             const unsigned og = xb_add(&bar[XB_TOP], 1u);
;             const unsigned tg = og / nx;
;             if (og + 1u == (tg + 1u) * nx) xb_add(&bar[XB_TOPGEN], 1u);
;             else XB_SPIN(xb_ld(&bar[XB_TOPGEN]) == tg, bar);
;             __builtin_amdgcn_fence(__ATOMIC_ACQUIRE, "agent");
;             xb_add(&bar[XB_XGEN(b.x)], 1u);
;             asm volatile("s_waitcnt vmcnt(0)" ::: "memory");
;         } else {
;             XB_SPIN(xb_ld(&bar[XB_XGEN(b.x)]) == gen, bar);
;             __builtin_amdgcn_fence(__ATOMIC_ACQUIRE, "agent");
;             asm volatile("s_waitcnt vmcnt(0)" ::: "memory");
.LBB0_802:
	s_or_b64 exec, exec, s[10:11]
	v_cvt_f32_u32_e32 v4, v2
	s_waitcnt vmcnt(0)
	v_readfirstlane_b32 s8, v3
	v_sub_u32_e32 v3, 0, v2
	v_rcp_iflag_f32_e32 v4, v4
	v_add_u32_e32 v5, s8, v1
	v_mul_f32_e32 v4, 0x4f7ffffe, v4
	v_cvt_u32_f32_e32 v4, v4
	v_mul_lo_u32 v1, v3, v4
	v_mul_hi_u32 v1, v4, v1
	v_add_u32_e32 v1, v4, v1
	v_mul_hi_u32 v1, v5, v1
	v_mul_lo_u32 v3, v1, v2
	v_sub_u32_e32 v3, v5, v3
	v_add_u32_e32 v4, 1, v1
	v_cmp_ge_u32_e32 vcc, v3, v2
	s_nop 1
	v_cndmask_b32_e32 v1, v1, v4, vcc
	v_sub_u32_e32 v4, v3, v2
	v_cndmask_b32_e32 v3, v3, v4, vcc
	v_add_u32_e32 v4, 1, v1
	v_cmp_ge_u32_e32 vcc, v3, v2
	v_add_u32_e32 v3, 1, v5
	s_nop 0
	v_cndmask_b32_e32 v1, v1, v4, vcc
	v_mul_lo_u32 v4, v2, v1
	v_add_u32_e32 v2, v4, v2
	s_waitcnt lgkmcnt(0)
	v_add_u32_e32 v4, 1, v1
	v_mul_lo_u32 v4, v4, v0
	v_mov_b32_e32 v5, 0x3000
	v_cmp_ne_u32_e32 vcc, v3, v2
	s_cbranch_vccnz .Lgb5_wait
	buffer_wbl2 sc1
	s_waitcnt vmcnt(0) lgkmcnt(0)
	v_mov_b32_e32 v2, 1
	global_atomic_add v5, v2, s[26:27] offset:1024
.Lgb5_wait:
	s_mov_b32 s28, 0
.Lgb5_spin:
	global_load_dword v3, v5, s[26:27] offset:1024 sc1
	s_waitcnt vmcnt(0)
	v_cmp_ge_u32_e32 vcc, v3, v4
	s_cbranch_vccnz .Lgb5_done
	s_sleep 1
	s_add_i32 s28, s28, 1
	s_cmp_lt_u32 s28, 0x8000
	s_cbranch_scc1 .Lgb5_spin

; __device__ __forceinline__ unsigned xb_ld(unsigned* p)              { return __hip_atomic_load(p, __ATOMIC_RELAXED, __HIP_MEMORY_SCOPE_AGENT); }
; __device__ __forceinline__ unsigned xb_add(unsigned* p, unsigned v) { return __hip_atomic_fetch_add(p, v, __ATOMIC_RELAXED, __HIP_MEMORY_SCOPE_AGENT); }
; #define XB_SPIN(cond, bar) do { unsigned _sp = 0; while (cond) { __builtin_amdgcn_s_sleep(1); \
;     if ((++_sp & 255u) == 0u) { if (xb_ld(&(bar)[XB_TMO])) break; if (_sp > XB_SPIN_CAP) { atomicAdd(&(bar)[XB_TMO], 1u); break; } } } } while (0)
; __device__ __forceinline__ void xcd_barrier(const XcdBarrier& b, const int tid) {
;     ...
;             else XB_SPIN(xb_ld(&bar[XB_TOPGEN]) == tg, bar);
;             __builtin_amdgcn_fence(__ATOMIC_ACQUIRE, "agent");
;             xb_add(&bar[XB_XGEN(b.x)], 1u);
;             asm volatile("s_waitcnt vmcnt(0)" ::: "memory");
;         } else {
;             XB_SPIN(xb_ld(&bar[XB_XGEN(b.x)]) == gen, bar);
;             __builtin_amdgcn_fence(__ATOMIC_ACQUIRE, "agent");
;             asm volatile("s_waitcnt vmcnt(0)" ::: "memory");
;         }
;     }
;     __syncthreads();
.Lgb5_out:
	s_waitcnt vmcnt(0)
.LBB0_836:
	s_or_b64 exec, exec, s[4:5]
	s_waitcnt lgkmcnt(0)
	s_barrier

; __device__ __forceinline__ unsigned xb_ld(unsigned* p)              { return __hip_atomic_load(p, __ATOMIC_RELAXED, __HIP_MEMORY_SCOPE_AGENT); }
; __device__ __forceinline__ unsigned xb_add(unsigned* p, unsigned v) { return __hip_atomic_fetch_add(p, v, __ATOMIC_RELAXED, __HIP_MEMORY_SCOPE_AGENT); }
; #define XB_SPIN(cond, bar) do { unsigned _sp = 0; while (cond) { __builtin_amdgcn_s_sleep(1); \
;     if ((++_sp & 255u) == 0u) { if (xb_ld(&(bar)[XB_TMO])) break; if (_sp > XB_SPIN_CAP) { atomicAdd(&(bar)[XB_TMO], 1u); break; } } } } while (0)
; __device__ __forceinline__ void xcd_barrier(const XcdBarrier& b, const int tid) {
;     ...
;             else XB_SPIN(xb_ld(&bar[XB_TOPGEN]) == tg, bar);
;             __builtin_amdgcn_fence(__ATOMIC_ACQUIRE, "agent");
;             xb_add(&bar[XB_XGEN(b.x)], 1u);
;             asm volatile("s_waitcnt vmcnt(0)" ::: "memory");
;         } else {
;             XB_SPIN(xb_ld(&bar[XB_XGEN(b.x)]) == gen, bar);
;             __builtin_amdgcn_fence(__ATOMIC_ACQUIRE, "agent");
;             asm volatile("s_waitcnt vmcnt(0)" ::: "memory");
;         }
;     }
;     __syncthreads();
.Lgb6_out:
	s_waitcnt vmcnt(0)
.LBB0_908:
	s_or_b64 exec, exec, s[0:1]
	s_waitcnt lgkmcnt(0)
	s_barrier
